# MLA steady loops: waves 0-3 (which have ~280 cycles of barrier slack) issue the LDS-DMA pieces of waves 4-7 as well; waves 4-7 issue none
# baseline (speedup 1.0000x reference)
; template <bool FOX>
; __device__ __forceinline__ void attn_unit(const Args& A, int b, int h, int qb, LAS char* shm, LAS float* dg) {
;     ...
;     const bf16_t* Kg = (FOX ? A.Fk : A.Kmla) + (long)(b * 8 + h) * 128 * (KSLOT / 2) + wid * 512 + lane * 8;
;     const bf16_t* Vg = (FOX ? A.Fv : A.Vmla) + (long)(b * 8 + h) * 128 * 4096 + wid * 512 + lane * 8;
;     const unsigned kdst = lds0 + L_K + wid * 1024, vdst = lds0 + L_V + wid * 1024;
;     const bool k2 = (!FOX) && wid < 4;
.LBB0_825:
	s_add_i32 s27, s26, 3
	s_cmp_lt_u32 s27, s94
	s_cbranch_scc0 .LBB0_828
	s_cmp_lg_u32 s98, 0
	s_cbranch_scc0 .Lmla_ss_no
	s_cmp_lg_u32 s26, s59
	s_cbranch_scc0 .Lmla_ss_no
	s_and_b32 s52, s27, 3
	s_mulk_i32 s52, 0x3000
	s_add_i32 s52, s52, s91
	s_add_i32 s53, s42, 0x6000
	s_and_b32 s53, s53, 0x6000
	s_add_i32 s53, s53, s93
	v_readfirstlane_b32 s46, v234
	v_readfirstlane_b32 s47, v235
	v_readfirstlane_b32 s60, v232
	v_readfirstlane_b32 s61, v233
	s_nop 3
	v_subrev_u32_e32 v240, s46, v234
	v_add_u32_e32 v241, 0x1000, v240
	s_add_u32 s98, s46, s56
	s_addc_u32 s99, s47, s57
	s_add_u32 s60, s60, s42
	s_addc_u32 s61, s61, s43
	s_nop 4
	s_cmp_lt_i32 s89, 4
	s_cbranch_scc1 .Lmla_ss1_in
	s_branch .Lmla_ss2_top

; template <bool FOX>
; __device__ __forceinline__ void attn_unit(const Args& A, int b, int h, int qb, LAS char* shm, LAS float* dg) {
;     ...
;     for (int t = 1; t < t_end; ++t) {
;         if (t == 1 && 4 < nti) ISSUE_K(t0 + 4, 0);
;         if (t + 4 < nti) ISSUE_K(t0 + t + 4, t % NS);
;         if (t + 2 < nti) ISSUE_V(t0 + t + 2, (t + 2) % NS);
;         SFENCE();
;         { if constexpr (!FOX) { if (t0 + t == tw_last + 1) {
; #pragma unroll
;                   for (int r = 0; r < 16; ++r) negm[r] = -INFINITY;
;                   asm volatile("" : "+v"(negm)); } }
;           const lds_cptr vp = vp0 + ((t - 1) % NS) * VSLOT; float sa = 0.f, sb = 0.f;
; #pragma unroll
;           for (int g = 0; g < 2 * NQ; ++g) {
;               if (!FOX && g == 0) c0 = __builtin_amdgcn_mfma_f32_32x32x16_bf16(kf[0], qr[0], negm, 0, 0, 0);
;               else if (!FOX && g == 1) c1 = __builtin_amdgcn_mfma_f32_32x32x16_bf16(kf[1], qr[0], negm, 0, 0, 0);
;               else if (g & 1) c1 = __builtin_amdgcn_mfma_f32_32x32x16_bf16(kf[g], qr[g >> 1], c1, 0, 0, 0); else c0 = __builtin_amdgcn_mfma_f32_32x32x16_bf16(kf[g], qr[g >> 1], c0, 0, 0, 0);
;               if (g < 8) { const int i = (g >> 1) + 4 * (g & 1); vlo[i] = vtr(vp + (i >> 2) * 4096 + (i & 3) * 1024); vhi[i] = vtr(vp + (i >> 2) * 4096 + (i & 3) * 1024 + 512);
;                   if (g < 4) { sa += pp0[4 * g]; sb += pp0[4 * g + 1]; sa += pp0[4 * g + 2]; sb += pp0[4 * g + 3]; } else { sa += pp1[4 * g - 16]; sb += pp1[4 * g - 15]; sa += pp1[4 * g - 14]; sb += pp1[4 * g - 13]; }
;                   asm volatile("" : "+v"(sa), "+v"(sb)); }
;               { constexpr int G0 = FOX ? 0 : 4; if (g >= G0) { const int q = 2 * (g - G0);
; #pragma unroll
;                   for (int k = 0; k < 2; ++k) { const int w = q + k; const unsigned pkd = w < 8 ? cvt_pk_bf16(pp0[2 * w], pp0[2 * w + 1]) : cvt_pk_bf16(pp1[2 * w - 16], pp1[2 * w - 15]); pw[w >> 2][w & 3] = pkd; } } }
;               SFENCE();
;           }
;           lrun += sa + sb; }
;         MASKONLY(t);
;         float rm; ROWMAX(rm);
;         bool resc = false;
;         if (__any(rm > THR)) { const float dl = fmaxf(rm, 0.f); mhat += dl;
; #pragma unroll
;             for (int r = 0; r < 16; ++r) { c0[r] -= dl; c1[r] -= dl; }
;             if constexpr (!FOX) {
; #pragma unroll
;                 for (int r = 0; r < 16; ++r) negm[r] = -mhat;
.Lmla_ss1_top:
	s_waitcnt vmcnt(6)
	s_barrier
.Lmla_ss1_in:
	s_mov_b32 m0, s52
	s_nop 0
	global_load_lds_dwordx4 v240, s[46:47]
	s_add_i32 m0, s52, 0x2000
	s_nop 0
	global_load_lds_dwordx4 v240, s[98:99]
	s_add_i32 m0, s52, 0x1000
	s_nop 0
	global_load_lds_dwordx4 v241, s[46:47]
	s_mov_b32 m0, s53
	s_nop 0
	global_load_lds_dwordx4 v240, s[60:61]
	s_add_i32 m0, s53, 0x1000
	s_nop 0
	global_load_lds_dwordx4 v241, s[60:61]
	s_waitcnt lgkmcnt(0)
	s_add_i32 s27, s42, 0x8000
	v_mfma_f32_32x32x16_bf16 v[114:129], v[206:209], v[138:141], v[82:97]
	s_and_b32 s27, s27, 0x6000
	s_add_u32 s42, s42, 0x2000
	s_addc_u32 s43, s43, 0
	v_add_u32_e32 v3, s27, v247
	ds_read_b64_tr_b16 v[206:207], v3 offset:49152
	ds_read_b64_tr_b16 v[208:209], v3 offset:49664
	v_add_f32_e32 v4, 0, v67
	v_add_f32_e32 v5, 0, v66
	v_add_f32_e32 v4, v69, v4
	v_add_f32_e32 v5, v68, v5
	v_mfma_f32_32x32x16_bf16 v[98:113], v[194:197], v[138:141], v[82:97]
	ds_read_b64_tr_b16 v[194:195], v3 offset:53248
	ds_read_b64_tr_b16 v[196:197], v3 offset:53760
	v_add_f32_e32 v4, v71, v4
	v_add_f32_e32 v5, v70, v5
	v_add_f32_e32 v4, v73, v4
	v_add_f32_e32 v5, v72, v5
	v_mfma_f32_32x32x16_bf16 v[114:129], v[202:205], v[142:145], v[114:129]
	ds_read_b64_tr_b16 v[202:203], v3 offset:50176
	ds_read_b64_tr_b16 v[204:205], v3 offset:50688
	v_add_f32_e32 v4, v75, v4
	v_add_f32_e32 v5, v74, v5
	v_add_f32_e32 v4, v77, v4
	v_add_f32_e32 v5, v76, v5
	v_mfma_f32_32x32x16_bf16 v[98:113], v[186:189], v[142:145], v[98:113]
	ds_read_b64_tr_b16 v[214:215], v3 offset:54272
	ds_read_b64_tr_b16 v[216:217], v3 offset:54784
	v_add_f32_e32 v4, v79, v4
	v_add_f32_e32 v5, v78, v5
	v_add_f32_e32 v4, v81, v4
	v_add_f32_e32 v5, v80, v5
	v_mfma_f32_32x32x16_bf16 v[114:129], v[198:201], v[146:149], v[114:129]
	ds_read_b64_tr_b16 v[210:211], v3 offset:51200
	ds_read_b64_tr_b16 v[212:213], v3 offset:51712
	v_add_f32_e32 v4, v51, v4
	v_add_f32_e32 v5, v50, v5
	v_add_f32_e32 v4, v53, v4
	v_add_f32_e32 v5, v52, v5
	v_mfma_f32_32x32x16_bf16 v[98:113], v[182:185], v[146:149], v[98:113]
	ds_read_b64_tr_b16 v[12:13], v3 offset:55296
	ds_read_b64_tr_b16 v[14:15], v3 offset:55808
	v_add_f32_e32 v4, v55, v4
	v_add_f32_e32 v5, v54, v5
	v_add_f32_e32 v4, v57, v4
	v_add_f32_e32 v5, v56, v5
	v_mfma_f32_32x32x16_bf16 v[114:129], v[190:193], v[150:153], v[114:129]
	ds_read_b64_tr_b16 v[8:9], v3 offset:52224
	ds_read_b64_tr_b16 v[10:11], v3 offset:52736
	v_add_f32_e32 v4, v59, v4
	v_add_f32_e32 v16, v61, v4
	v_add_f32_e32 v4, v58, v5
	v_add_f32_e32 v17, v60, v4
	v_mfma_f32_32x32x16_bf16 v[98:113], v[170:173], v[150:153], v[98:113]
	s_add_u32 s46, s46, s62
	s_addc_u32 s47, s47, s63
	s_and_b32 s64, s26, 3
	ds_read_b64_tr_b16 v[4:5], v3 offset:56320
	ds_read_b64_tr_b16 v[6:7], v3 offset:56832
	v_add_f32_e32 v3, v63, v16
	v_add_f32_e32 v16, v62, v17
	v_add_f32_e32 v3, v65, v3
	v_add_f32_e32 v16, v64, v16
	v_mfma_f32_32x32x16_bf16 v[114:129], v[178:181], v[154:157], v[114:129]
	s_mulk_i32 s64, 0x3000
	s_add_u32 s60, s60, 0x2000
	s_addc_u32 s61, s61, 0
	v_cvt_pk_bf16_f32 v178, v50, v51
	v_cvt_pk_bf16_f32 v179, v52, v53
	v_cvt_pk_bf16_f32 v186, v66, v67
	v_cvt_pk_bf16_f32 v187, v68, v69
	v_mfma_f32_32x32x16_bf16 v[98:113], v[166:169], v[154:157], v[98:113]
	s_add_i32 s52, s64, s91
	s_add_i32 s64, s42, 0x6000
	s_add_u32 s98, s98, s62
	s_addc_u32 s99, s99, s63
	v_cvt_pk_bf16_f32 v180, v54, v55
	v_cvt_pk_bf16_f32 v181, v56, v57
	v_cvt_pk_bf16_f32 v188, v70, v71
	v_cvt_pk_bf16_f32 v189, v72, v73
	v_mfma_f32_32x32x16_bf16 v[114:129], v[174:177], v[158:161], v[114:129]
	s_and_b32 s64, s64, 0x6000
	s_add_i32 s53, s64, s93
	v_cvt_pk_bf16_f32 v218, v58, v59
	v_cvt_pk_bf16_f32 v219, v60, v61
	v_cvt_pk_bf16_f32 v182, v74, v75
	v_cvt_pk_bf16_f32 v183, v76, v77
	v_mfma_f32_32x32x16_bf16 v[98:113], v[162:165], v[158:161], v[98:113]
	v_cvt_pk_bf16_f32 v220, v62, v63
	v_cvt_pk_bf16_f32 v221, v64, v65
	v_cvt_pk_bf16_f32 v184, v78, v79
	v_cvt_pk_bf16_f32 v185, v80, v81
	v_add_f32_e32 v3, v3, v16
	v_add_f32_e32 v246, v246, v3
	s_nop 3
	s_waitcnt lgkmcnt(0)
	v_mfma_f32_32x32x16_bf16 v[18:33], v[186:189], v[206:209], v[18:33]
	s_add_i32 s27, s26, 1
	s_and_b32 s64, s27, 3
	s_mulk_i32 s64, 0x3000
	v_exp_f32_e32 v66, v114
	v_exp_f32_e32 v67, v115
	v_exp_f32_e32 v68, v116
	v_exp_f32_e32 v69, v117
	v_add_u32_e32 v3, s64, v248
	v_mfma_f32_32x32x16_bf16 v[34:49], v[186:189], v[194:197], v[34:49]
	v_exp_f32_e32 v70, v118
	v_exp_f32_e32 v71, v119
	v_exp_f32_e32 v72, v120
	v_exp_f32_e32 v73, v121
	ds_read_b128 v[206:209], v3
	ds_read_b128 v[194:197], v3 offset:512
	v_mfma_f32_32x32x16_bf16 v[18:33], v[182:185], v[202:205], v[18:33]
	v_exp_f32_e32 v74, v122
	v_exp_f32_e32 v75, v123
	v_exp_f32_e32 v76, v124
	v_exp_f32_e32 v77, v125
	ds_read_b128 v[202:205], v3 offset:2048
	ds_read_b128 v[186:189], v3 offset:2560
	v_mfma_f32_32x32x16_bf16 v[34:49], v[182:185], v[214:217], v[34:49]
	v_exp_f32_e32 v78, v126
	v_exp_f32_e32 v79, v127
	v_exp_f32_e32 v80, v128
	v_exp_f32_e32 v81, v129
	ds_read_b128 v[198:201], v3 offset:4096
	ds_read_b128 v[182:185], v3 offset:4608
	v_mfma_f32_32x32x16_bf16 v[18:33], v[178:181], v[210:213], v[18:33]
	v_exp_f32_e32 v50, v98
	v_exp_f32_e32 v51, v99
	v_exp_f32_e32 v52, v100
	v_exp_f32_e32 v53, v101
	ds_read_b128 v[190:193], v3 offset:6144
	ds_read_b128 v[170:173], v3 offset:6656
	v_mfma_f32_32x32x16_bf16 v[34:49], v[178:181], v[12:15], v[34:49]
	v_exp_f32_e32 v54, v102
	v_exp_f32_e32 v55, v103
	v_exp_f32_e32 v56, v104
	v_exp_f32_e32 v57, v105
	ds_read_b128 v[178:181], v3 offset:8192
	ds_read_b128 v[166:169], v3 offset:8704
	v_mfma_f32_32x32x16_bf16 v[18:33], v[218:221], v[8:11], v[18:33]
	v_exp_f32_e32 v58, v106
	v_exp_f32_e32 v59, v107
	v_exp_f32_e32 v60, v108
	v_exp_f32_e32 v61, v109
	ds_read_b128 v[174:177], v3 offset:10240
	ds_read_b128 v[162:165], v3 offset:10752
	v_mfma_f32_32x32x16_bf16 v[34:49], v[218:221], v[4:7], v[34:49]
	v_exp_f32_e32 v62, v110
	v_exp_f32_e32 v63, v111
	v_exp_f32_e32 v64, v112
	v_exp_f32_e32 v65, v113
	s_mov_b32 s26, s27
	s_cmp_eq_u32 s27, s96
	s_cbranch_scc1 .Lmla_ss1_xdone
	s_add_i32 s64, s27, 3
	s_cmp_lt_u32 s64, s94
	s_cbranch_scc1 .Lmla_ss1_top
	s_waitcnt vmcnt(6)
	s_barrier
	s_branch .Lmla_ss_back
; template <bool FOX>
; __device__ __forceinline__ void attn_unit(const Args& A, int b, int h, int qb, LAS char* shm, LAS float* dg) {
;     ...
;         { if constexpr (!FOX) { if (t0 + t == tw_last + 1) {
; #pragma unroll
;                   for (int r = 0; r < 16; ++r) negm[r] = -INFINITY;
;                   asm volatile("" : "+v"(negm)); } }
;           const lds_cptr vp = vp0 + ((t - 1) % NS) * VSLOT; float sa = 0.f, sb = 0.f;
; #pragma unroll
;           for (int g = 0; g < 2 * NQ; ++g) {
;               if (!FOX && g == 0) c0 = __builtin_amdgcn_mfma_f32_32x32x16_bf16(kf[0], qr[0], negm, 0, 0, 0);
;               else if (!FOX && g == 1) c1 = __builtin_amdgcn_mfma_f32_32x32x16_bf16(kf[1], qr[0], negm, 0, 0, 0);
;               else if (g & 1) c1 = __builtin_amdgcn_mfma_f32_32x32x16_bf16(kf[g], qr[g >> 1], c1, 0, 0, 0); else c0 = __builtin_amdgcn_mfma_f32_32x32x16_bf16(kf[g], qr[g >> 1], c0, 0, 0, 0);
;               if (g < 8) { const int i = (g >> 1) + 4 * (g & 1); vlo[i] = vtr(vp + (i >> 2) * 4096 + (i & 3) * 1024); vhi[i] = vtr(vp + (i >> 2) * 4096 + (i & 3) * 1024 + 512);
;                   if (g < 4) { sa += pp0[4 * g]; sb += pp0[4 * g + 1]; sa += pp0[4 * g + 2]; sb += pp0[4 * g + 3]; } else { sa += pp1[4 * g - 16]; sb += pp1[4 * g - 15]; sa += pp1[4 * g - 14]; sb += pp1[4 * g - 13]; }
;                   asm volatile("" : "+v"(sa), "+v"(sb)); }
;               { constexpr int G0 = FOX ? 0 : 4; if (g >= G0) { const int q = 2 * (g - G0);
; #pragma unroll
;                   for (int k = 0; k < 2; ++k) { const int w = q + k; const unsigned pkd = w < 8 ? cvt_pk_bf16(pp0[2 * w], pp0[2 * w + 1]) : cvt_pk_bf16(pp1[2 * w - 16], pp1[2 * w - 15]); pw[w >> 2][w & 3] = pkd; } } }
;               SFENCE();
;           }
;           lrun += sa + sb; }
;         MASKONLY(t);
;         float rm; ROWMAX(rm);
;         bool resc = false;
;         if (__any(rm > THR)) { const float dl = fmaxf(rm, 0.f); mhat += dl;
; #pragma unroll
;             for (int r = 0; r < 16; ++r) { c0[r] -= dl; c1[r] -= dl; }
;             if constexpr (!FOX) {
; #pragma unroll
;                 for (int r = 0; r < 16; ++r) negm[r] = -mhat;
;                 asm volatile("" : "+v"(negm)); }
;             const float f = __builtin_amdgcn_exp2f(-dl); lrun *= f; if (hi == 0) wsf[r32] = f; resc = true; }
;         SFENCE();
;         { const lds_cptr kp = kp0 + ((t + 1) % NS) * KSLOT;
.Lmla_ss1_xdone:
	s_waitcnt vmcnt(6)
	s_barrier
	s_branch .Lmla_ss_done
	.p2alignl 6, 3212836864
.Lmla_ss2_top:
	s_waitcnt lgkmcnt(0)
	s_add_i32 s27, s42, 0x8000
	v_mfma_f32_32x32x16_bf16 v[114:129], v[206:209], v[138:141], v[82:97]
	s_and_b32 s27, s27, 0x6000
	s_add_u32 s42, s42, 0x2000
	s_addc_u32 s43, s43, 0
	v_add_u32_e32 v3, s27, v247
	ds_read_b64_tr_b16 v[206:207], v3 offset:49152
	ds_read_b64_tr_b16 v[208:209], v3 offset:49664
	v_add_f32_e32 v4, 0, v67
	v_add_f32_e32 v5, 0, v66
	v_add_f32_e32 v4, v69, v4
	v_add_f32_e32 v5, v68, v5
	v_mfma_f32_32x32x16_bf16 v[98:113], v[194:197], v[138:141], v[82:97]
	ds_read_b64_tr_b16 v[194:195], v3 offset:53248
	ds_read_b64_tr_b16 v[196:197], v3 offset:53760
	v_add_f32_e32 v4, v71, v4
	v_add_f32_e32 v5, v70, v5
	v_add_f32_e32 v4, v73, v4
	v_add_f32_e32 v5, v72, v5
	v_mfma_f32_32x32x16_bf16 v[114:129], v[202:205], v[142:145], v[114:129]
	ds_read_b64_tr_b16 v[202:203], v3 offset:50176
	ds_read_b64_tr_b16 v[204:205], v3 offset:50688
	v_add_f32_e32 v4, v75, v4
	v_add_f32_e32 v5, v74, v5
	v_add_f32_e32 v4, v77, v4
	v_add_f32_e32 v5, v76, v5
	v_mfma_f32_32x32x16_bf16 v[98:113], v[186:189], v[142:145], v[98:113]
	ds_read_b64_tr_b16 v[214:215], v3 offset:54272
	ds_read_b64_tr_b16 v[216:217], v3 offset:54784
	v_add_f32_e32 v4, v79, v4
	v_add_f32_e32 v5, v78, v5
	v_add_f32_e32 v4, v81, v4
	v_add_f32_e32 v5, v80, v5
	v_mfma_f32_32x32x16_bf16 v[114:129], v[198:201], v[146:149], v[114:129]
	ds_read_b64_tr_b16 v[210:211], v3 offset:51200
	ds_read_b64_tr_b16 v[212:213], v3 offset:51712
	v_add_f32_e32 v4, v51, v4
	v_add_f32_e32 v5, v50, v5
	v_add_f32_e32 v4, v53, v4
	v_add_f32_e32 v5, v52, v5
	v_mfma_f32_32x32x16_bf16 v[98:113], v[182:185], v[146:149], v[98:113]
	ds_read_b64_tr_b16 v[12:13], v3 offset:55296
	ds_read_b64_tr_b16 v[14:15], v3 offset:55808
	v_add_f32_e32 v4, v55, v4
	v_add_f32_e32 v5, v54, v5
	v_add_f32_e32 v4, v57, v4
	v_add_f32_e32 v5, v56, v5
	v_mfma_f32_32x32x16_bf16 v[114:129], v[190:193], v[150:153], v[114:129]
	ds_read_b64_tr_b16 v[8:9], v3 offset:52224
	ds_read_b64_tr_b16 v[10:11], v3 offset:52736
	v_add_f32_e32 v4, v59, v4
	v_add_f32_e32 v16, v61, v4
	v_add_f32_e32 v4, v58, v5
	v_add_f32_e32 v17, v60, v4
	v_mfma_f32_32x32x16_bf16 v[98:113], v[170:173], v[150:153], v[98:113]
	s_add_u32 s46, s46, s62
	s_addc_u32 s47, s47, s63
	ds_read_b64_tr_b16 v[4:5], v3 offset:56320
	ds_read_b64_tr_b16 v[6:7], v3 offset:56832
	v_add_f32_e32 v3, v63, v16
	v_add_f32_e32 v16, v62, v17
	v_add_f32_e32 v3, v65, v3
	v_add_f32_e32 v16, v64, v16
	v_mfma_f32_32x32x16_bf16 v[114:129], v[178:181], v[154:157], v[114:129]
	v_cvt_pk_bf16_f32 v178, v50, v51
	v_cvt_pk_bf16_f32 v179, v52, v53
	v_cvt_pk_bf16_f32 v186, v66, v67
	v_cvt_pk_bf16_f32 v187, v68, v69
	v_mfma_f32_32x32x16_bf16 v[98:113], v[166:169], v[154:157], v[98:113]
	v_cvt_pk_bf16_f32 v180, v54, v55
	v_cvt_pk_bf16_f32 v181, v56, v57
	v_cvt_pk_bf16_f32 v188, v70, v71
	v_cvt_pk_bf16_f32 v189, v72, v73
	v_mfma_f32_32x32x16_bf16 v[114:129], v[174:177], v[158:161], v[114:129]
	v_cvt_pk_bf16_f32 v218, v58, v59
	v_cvt_pk_bf16_f32 v219, v60, v61
	v_cvt_pk_bf16_f32 v182, v74, v75
	v_cvt_pk_bf16_f32 v183, v76, v77
	v_mfma_f32_32x32x16_bf16 v[98:113], v[162:165], v[158:161], v[98:113]
	v_cvt_pk_bf16_f32 v220, v62, v63
	v_cvt_pk_bf16_f32 v221, v64, v65
	v_cvt_pk_bf16_f32 v184, v78, v79
	v_cvt_pk_bf16_f32 v185, v80, v81
	v_add_f32_e32 v3, v3, v16
	v_add_f32_e32 v246, v246, v3
	s_waitcnt vmcnt(0)
	s_waitcnt lgkmcnt(0)
	s_barrier
	v_mfma_f32_32x32x16_bf16 v[18:33], v[186:189], v[206:209], v[18:33]
	s_add_i32 s27, s26, 1
	s_and_b32 s64, s27, 3
	s_mulk_i32 s64, 0x3000
	v_exp_f32_e32 v66, v114
	v_exp_f32_e32 v67, v115
	v_exp_f32_e32 v68, v116
	v_exp_f32_e32 v69, v117
	v_add_u32_e32 v3, s64, v248
	v_mfma_f32_32x32x16_bf16 v[34:49], v[186:189], v[194:197], v[34:49]
	v_exp_f32_e32 v70, v118
	v_exp_f32_e32 v71, v119
	v_exp_f32_e32 v72, v120
	v_exp_f32_e32 v73, v121
	ds_read_b128 v[206:209], v3
	ds_read_b128 v[194:197], v3 offset:512
	v_mfma_f32_32x32x16_bf16 v[18:33], v[182:185], v[202:205], v[18:33]
	v_exp_f32_e32 v74, v122
	v_exp_f32_e32 v75, v123
	v_exp_f32_e32 v76, v124
	v_exp_f32_e32 v77, v125
	ds_read_b128 v[202:205], v3 offset:2048
	ds_read_b128 v[186:189], v3 offset:2560
	v_mfma_f32_32x32x16_bf16 v[34:49], v[182:185], v[214:217], v[34:49]
	v_exp_f32_e32 v78, v126
	v_exp_f32_e32 v79, v127
	v_exp_f32_e32 v80, v128
	v_exp_f32_e32 v81, v129
	ds_read_b128 v[198:201], v3 offset:4096
	ds_read_b128 v[182:185], v3 offset:4608
	v_mfma_f32_32x32x16_bf16 v[18:33], v[178:181], v[210:213], v[18:33]
	v_exp_f32_e32 v50, v98
	v_exp_f32_e32 v51, v99
	v_exp_f32_e32 v52, v100
	v_exp_f32_e32 v53, v101
	ds_read_b128 v[190:193], v3 offset:6144
	ds_read_b128 v[170:173], v3 offset:6656
	v_mfma_f32_32x32x16_bf16 v[34:49], v[178:181], v[12:15], v[34:49]
	v_exp_f32_e32 v54, v102
	v_exp_f32_e32 v55, v103
	v_exp_f32_e32 v56, v104
	v_exp_f32_e32 v57, v105
	ds_read_b128 v[178:181], v3 offset:8192
	ds_read_b128 v[166:169], v3 offset:8704
	v_mfma_f32_32x32x16_bf16 v[18:33], v[218:221], v[8:11], v[18:33]
	v_exp_f32_e32 v58, v106
	v_exp_f32_e32 v59, v107
	v_exp_f32_e32 v60, v108
	v_exp_f32_e32 v61, v109
	ds_read_b128 v[174:177], v3 offset:10240
	ds_read_b128 v[162:165], v3 offset:10752
	v_mfma_f32_32x32x16_bf16 v[34:49], v[218:221], v[4:7], v[34:49]
	v_exp_f32_e32 v62, v110
	v_exp_f32_e32 v63, v111
	v_exp_f32_e32 v64, v112
	v_exp_f32_e32 v65, v113
	s_mov_b32 s26, s27
	s_cmp_eq_u32 s27, s96
	s_cbranch_scc1 .Lmla_ss2_xdone
	s_add_i32 s64, s27, 3
	s_cmp_lt_u32 s64, s94
	s_cbranch_scc1 .Lmla_ss2_top
	s_branch .Lmla_ss_back
